# bg_take claim prefetch (next step's atomic issued one step early) on top of two-site tail-fill
# baseline (speedup 1.0000x reference)
; #define LAS __attribute__((address_space(3)))
; #define PHASE_BEGIN() Ctx c = c0; { int t_ = c0.tid; asm volatile("" : "+v"(t_)); c.tid = t_; c.lane = t_ & 63; c.wave = __builtin_amdgcn_readfirstlane(t_ >> 6); } \
;     GAS unsigned char* wsb = (GAS unsigned char*)a.ws; asm volatile("" : "+s"(wsb));
; __device__ __forceinline__ void bg_take(const Args& a, const Ctx& c0, int n) {
;     PHASE_BEGIN();
;     unsigned* head = WSP(unsigned, WS_CTL) + CW_QHEAD;
;     volatile LAS unsigned* bc = (volatile LAS unsigned*)(c.lds + LDS_MISC + 64);
;     LAS float* scr = (LAS float*)(c.lds + c.wave * 16640);
;     __syncthreads();
.Lbal1_d:
.Lbt1_entry:
	v_mov_b32_e32 v2, v0
	v_readlane_b32 s8, v254, 21
	v_readlane_b32 s10, v254, 23
	v_readfirstlane_b32 s2, v2
	v_readlane_b32 s11, v254, 24
	s_ashr_i32 s15, s2, 6
	s_mov_b64 s[6:7], s[10:11]
	s_waitcnt lgkmcnt(0)
	v_lshlrev_b32_e32 v3, 2, v2
	s_add_u32 s2, s6, 0x8000
	s_mul_i32 s8, s15, 0x4100
	v_bfe_u32 v67, v2, 4, 2
	v_and_b32_e32 v66, 60, v3
	s_addc_u32 s3, s7, 0
	s_add_i32 s8, s8, 0
	v_cmp_eq_u32_e64 s[40:41], 0, v2
	v_mul_u32_u24_e32 v3, 0x104, v67
	v_lshlrev_b32_e32 v4, 2, v66
	v_bfe_u32 v96, v2, 3, 3
	v_lshlrev_b32_e32 v2, 3, v2
	v_add3_u32 v95, s8, v3, v4
	v_and_b32_e32 v2, 56, v2
	v_mov_b32_e32 v3, v147
	v_mul_u32_u24_e32 v6, 0x104, v2
	v_lshl_add_u64 v[4:5], s[6:7], 0, v[2:3]
	v_lshlrev_b32_e32 v3, 2, v96
	v_add3_u32 v97, s8, v6, v3
	v_lshlrev_b32_e32 v2, 1, v2
	v_mov_b32_e32 v3, v147
	v_lshl_add_u64 v[2:3], s[6:7], 0, v[2:3]
	s_mov_b64 s[6:7], 0x1bc00000
	v_lshl_add_u64 v[72:73], v[2:3], 0, s[6:7]
	s_mov_b64 s[6:7], 0x1b800000
	v_lshl_add_u64 v[74:75], v[2:3], 0, s[6:7]
	s_mov_b64 s[6:7], 0x1b600000
	v_lshl_add_u64 v[76:77], v[2:3], 0, s[6:7]
	s_mov_b64 s[6:7], 0x1aa00000
	v_lshl_add_u64 v[78:79], v[2:3], 0, s[6:7]
	s_mov_b64 s[6:7], 0x12a00000
	v_lshl_add_u64 v[80:81], v[4:5], 0, s[6:7]
	s_mov_b64 s[6:7], 0x2a00000
	v_lshl_add_u64 v[82:83], v[4:5], 0, s[6:7]
	s_mov_b64 s[6:7], 0x2200000
	v_lshl_add_u64 v[84:85], v[2:3], 0, s[6:7]
	s_mov_b64 s[6:7], 0x1e00000
	v_readlane_b32 s9, v254, 22
	v_lshl_add_u64 v[86:87], v[2:3], 0, s[6:7]
	s_mov_b64 s[6:7], 0x1c00000
	s_mov_b64 s[10:11], 0x2c400000
	s_mov_b64 s[8:9], 0x1c400000
	v_lshl_add_u64 v[88:89], v[2:3], 0, s[6:7]
	s_mov_b64 s[6:7], 0x1000000
	v_lshl_add_u64 v[68:69], v[4:5], 0, s[10:11]
	v_or_b32_e32 v98, 8, v96
	v_or_b32_e32 v99, 16, v96
	v_or_b32_e32 v100, 24, v96
	v_or_b32_e32 v101, 32, v96
	v_or_b32_e32 v102, 40, v96
	v_or_b32_e32 v103, 48, v96
	v_or_b32_e32 v104, 56, v96
	v_lshl_add_u64 v[70:71], v[4:5], 0, s[8:9]
	v_lshl_add_u64 v[90:91], v[2:3], 0, s[6:7]
	s_waitcnt vmcnt(0)
	s_barrier
	v_writelane_b32 v255, 0, 40
	s_branch .LBB0_1256

; __device__ __forceinline__ void bg_take(const Args& a, const Ctx& c0, int n) {
;     ...
;     for (int i = 0; i < n; ++i) {
;         if (c.tid == 0) { unsigned s = __hip_atomic_fetch_add(head, 1u, __ATOMIC_RELAXED, __HIP_MEMORY_SCOPE_AGENT); if (s >= (unsigned)BG_STEPS) s = 0xffffffffu; bc[0] = s; }
;         __syncthreads();
.LBB0_1256:
	s_and_saveexec_b64 s[6:7], s[40:41]
	s_cbranch_execz .LBB0_1260
	s_mov_b64 s[10:11], exec
	v_mbcnt_lo_u32_b32 v2, s10, 0
	v_mbcnt_hi_u32_b32 v2, s11, v2
	v_cmp_eq_u32_e32 vcc, 0, v2
	s_and_saveexec_b64 s[8:9], vcc
	s_cbranch_execz .LBB0_1259
	v_readlane_b32 s10, v255, 40
	s_nop 3
	s_cmp_lg_u32 s10, 0
	s_cbranch_scc1 .Lpf1_have
	v_mov_b32_e32 v3, 1
	global_atomic_add v3, v147, v3, s[2:3] sc0
	s_waitcnt vmcnt(0)
	s_branch .Lpf1_next
.Lpf1_have:
	s_waitcnt vmcnt(0)
	v_mov_b32_e32 v3, v105
.Lpf1_next:
	v_writelane_b32 v255, 0, 40
	s_cmp_lt_u32 s14, 2
	s_cbranch_scc1 .Lpf1_done
	v_mov_b32_e32 v105, 1
	global_atomic_add v105, v147, v105, s[2:3] sc0
	v_writelane_b32 v255, 1, 40
.Lpf1_done:
.LBB0_1259:
	s_or_b64 exec, exec, s[8:9]
	v_readfirstlane_b32 s8, v3
	v_mov_b32_e32 v3, s76
	s_nop 0
	v_add_u32_e32 v2, s8, v2
	v_cmp_gt_u32_e32 vcc, s78, v2
	s_nop 1
	v_cndmask_b32_e32 v2, -1, v2, vcc
	ds_write_b32 v3, v2

; __device__ __forceinline__ void bg_take(const Args& a, const Ctx& c0, int n) {
;     ...
;         __syncthreads();
;     }
;     __syncthreads();
.LBB0_1441:
	s_waitcnt vmcnt(0)
	s_barrier
	v_readlane_b32 s2, v255, 42
	s_nop 3
	s_cmp_eq_u32 s2, 1
	s_cbranch_scc0 .Lbt1_notA
	v_writelane_b32 v255, 2, 42
	s_branch .LBB0_321

; #define LAS __attribute__((address_space(3)))
; #define PHASE_BEGIN() Ctx c = c0; { int t_ = c0.tid; asm volatile("" : "+v"(t_)); c.tid = t_; c.lane = t_ & 63; c.wave = __builtin_amdgcn_readfirstlane(t_ >> 6); } \
;     GAS unsigned char* wsb = (GAS unsigned char*)a.ws; asm volatile("" : "+s"(wsb));
; __device__ __forceinline__ void bg_take(const Args& a, const Ctx& c0, int n) {
;     PHASE_BEGIN();
;     unsigned* head = WSP(unsigned, WS_CTL) + CW_QHEAD;
;     volatile LAS unsigned* bc = (volatile LAS unsigned*)(c.lds + LDS_MISC + 64);
;     LAS float* scr = (LAS float*)(c.lds + c.wave * 16640);
;     __syncthreads();
.Lbal2_d:
	s_ashr_i32 s11, s2, 6
	s_mov_b64 s[4:5], s[6:7]
	v_lshlrev_b32_e32 v2, 2, v1
	s_add_u32 s2, s4, 0x8000
	s_mul_i32 s6, s11, 0x4100
	v_bfe_u32 v67, v1, 4, 2
	v_and_b32_e32 v66, 60, v2
	s_addc_u32 s3, s5, 0
	s_add_i32 s6, s6, 0
	v_cmp_eq_u32_e64 s[38:39], 0, v1
	v_mul_u32_u24_e32 v2, 0x104, v67
	s_waitcnt lgkmcnt(0)
	v_lshlrev_b32_e32 v3, 2, v66
	v_bfe_u32 v96, v1, 3, 3
	v_lshlrev_b32_e32 v1, 3, v1
	v_add3_u32 v95, s6, v2, v3
	v_and_b32_e32 v2, 56, v1
	v_mov_b32_e32 v3, v147
	v_mul_u32_u24_e32 v1, 0x104, v2
	v_lshl_add_u64 v[4:5], s[4:5], 0, v[2:3]
	v_lshlrev_b32_e32 v3, 2, v96
	v_add3_u32 v97, s6, v1, v3
	v_lshlrev_b32_e32 v2, 1, v2
	v_mov_b32_e32 v3, v147
	v_lshl_add_u64 v[2:3], s[4:5], 0, v[2:3]
	s_mov_b64 s[4:5], 0x1bc00000
	v_lshl_add_u64 v[72:73], v[2:3], 0, s[4:5]
	s_mov_b64 s[4:5], 0x1b800000
	v_lshl_add_u64 v[74:75], v[2:3], 0, s[4:5]
	s_mov_b64 s[4:5], 0x1b600000
	v_lshl_add_u64 v[76:77], v[2:3], 0, s[4:5]
	s_mov_b64 s[4:5], 0x1aa00000
	v_lshl_add_u64 v[78:79], v[2:3], 0, s[4:5]
	s_mov_b64 s[4:5], 0x12a00000
	v_lshl_add_u64 v[80:81], v[4:5], 0, s[4:5]
	s_mov_b64 s[4:5], 0x2a00000
	v_lshl_add_u64 v[82:83], v[4:5], 0, s[4:5]
	s_mov_b64 s[4:5], 0x2200000
	v_lshl_add_u64 v[84:85], v[2:3], 0, s[4:5]
	s_mov_b64 s[4:5], 0x1e00000
	v_lshl_add_u64 v[86:87], v[2:3], 0, s[4:5]
	s_mov_b64 s[4:5], 0x1c00000
	s_mov_b64 s[8:9], 0x2c400000
	s_mov_b64 s[6:7], 0x1c400000
	v_lshl_add_u64 v[88:89], v[2:3], 0, s[4:5]
	s_mov_b64 s[4:5], 0x1000000
	v_lshl_add_u64 v[68:69], v[4:5], 0, s[8:9]
	v_or_b32_e32 v98, 8, v96
	v_or_b32_e32 v99, 16, v96
	v_or_b32_e32 v100, 24, v96
	v_or_b32_e32 v101, 32, v96
	v_or_b32_e32 v102, 40, v96
	v_or_b32_e32 v103, 48, v96
	v_or_b32_e32 v104, 56, v96
	v_lshl_add_u64 v[70:71], v[4:5], 0, s[6:7]
	v_lshl_add_u64 v[90:91], v[2:3], 0, s[4:5]
	s_waitcnt vmcnt(0)
	s_barrier
	v_writelane_b32 v255, 0, 41
	s_branch .LBB0_1496

; __device__ __forceinline__ void bg_take(const Args& a, const Ctx& c0, int n) {
;     ...
;     for (int i = 0; i < n; ++i) {
;         if (c.tid == 0) { unsigned s = __hip_atomic_fetch_add(head, 1u, __ATOMIC_RELAXED, __HIP_MEMORY_SCOPE_AGENT); if (s >= (unsigned)BG_STEPS) s = 0xffffffffu; bc[0] = s; }
;         __syncthreads();
.LBB0_1496:
	s_and_saveexec_b64 s[4:5], s[38:39]
	s_cbranch_execz .LBB0_1500
	s_mov_b64 s[8:9], exec
	v_mbcnt_lo_u32_b32 v1, s8, 0
	v_mbcnt_hi_u32_b32 v2, s9, v1
	v_cmp_eq_u32_e32 vcc, 0, v2
	s_and_saveexec_b64 s[6:7], vcc
	s_cbranch_execz .LBB0_1499
	v_readlane_b32 s8, v255, 41
	s_nop 3
	s_cmp_lg_u32 s8, 0
	s_cbranch_scc1 .Lpf2_have
	v_mov_b32_e32 v3, 1
	global_atomic_add v3, v147, v3, s[2:3] sc0
	s_waitcnt vmcnt(0)
	s_branch .Lpf2_next

; __device__ __forceinline__ void bg_take(const Args& a, const Ctx& c0, int n) {
;     ...
;     for (int i = 0; i < n; ++i) {
;         if (c.tid == 0) { unsigned s = __hip_atomic_fetch_add(head, 1u, __ATOMIC_RELAXED, __HIP_MEMORY_SCOPE_AGENT); if (s >= (unsigned)BG_STEPS) s = 0xffffffffu; bc[0] = s; }
;         __syncthreads();
.Lpf2_next:
	v_writelane_b32 v255, 0, 41
	s_cmp_lt_u32 s10, 2
	s_cbranch_scc1 .Lpf2_done
	v_mov_b32_e32 v105, 1
	global_atomic_add v105, v147, v105, s[2:3] sc0
	v_writelane_b32 v255, 1, 41
.Lpf2_done:
.LBB0_1499:
	s_or_b64 exec, exec, s[6:7]
	v_readfirstlane_b32 s6, v3
	s_nop 1
	v_add_u32_e32 v1, s6, v2
	v_cmp_gt_u32_e32 vcc, s78, v1
	v_mov_b32_e32 v2, s76
	s_nop 0
	v_cndmask_b32_e32 v1, -1, v1, vcc
	ds_write_b32 v2, v1

; #define LAS __attribute__((address_space(3)))
; __device__ __forceinline__ float silu_(float x) { return x * sigmoid_(x); }
; #define PHASE_BEGIN() Ctx c = c0; { int t_ = c0.tid; asm volatile("" : "+v"(t_)); c.tid = t_; c.lane = t_ & 63; c.wave = __builtin_amdgcn_readfirstlane(t_ >> 6); } \
;     GAS unsigned char* wsb = (GAS unsigned char*)a.ws; asm volatile("" : "+s"(wsb));
; __device__ __forceinline__ void mod_items(const Args& a, const Ctx& c0, int l) {
;     PHASE_BEGIN();
;     __syncthreads();
;     LAS float* sc = (LAS float*)c.lds;
;     LAS float* red = (LAS float*)(c.lds + 40960);
;     for (int i = c.tid; i < 5 * DM; i += 512) { const int r = i >> 11, k = i & 2047; const float v = r < 4 ? INP(1)[r * DM + k] : INP(3)[k]; sc[i] = silu_(v); }
; __device__ __forceinline__ void bg_take(const Args& a, const Ctx& c0, int n) {
;     ...
;         __syncthreads();
;     }
;     __syncthreads();
.LBB0_1681:
	s_waitcnt vmcnt(0)
	v_readlane_b32 s2, v254, 54
	v_readlane_b32 s3, v254, 55
	s_andn2_b64 vcc, exec, s[2:3]
	s_barrier
	s_cbranch_vccnz .LBB0_1700
	v_readlane_b32 s4, v254, 21
	v_mov_b32_e32 v2, v0
	v_readlane_b32 s6, v254, 23
	v_readlane_b32 s7, v254, 24
	s_movk_i32 s4, 0x2800
	v_readlane_b32 s5, v254, 22
	s_mov_b64 s[2:3], s[6:7]
	v_cmp_gt_i32_e32 vcc, s4, v2
	s_barrier
	s_and_saveexec_b64 s[4:5], vcc
	v_readlane_b32 s40, v253, 52
	v_readlane_b32 s42, v253, 54
	v_readlane_b32 s43, v253, 55
	v_readlane_b32 s46, v253, 58
	v_readlane_b32 s47, v253, 59
	s_movk_i32 s10, 0x25ff
	s_mov_b64 s[14:15], 0x800
	v_readlane_b32 s41, v253, 53
	v_readlane_b32 s44, v253, 56
	v_readlane_b32 s45, v253, 57
	v_readlane_b32 s48, v253, 60
	v_readlane_b32 s49, v253, 61
	v_readlane_b32 s50, v253, 62
	v_readlane_b32 s51, v253, 63
	v_readlane_b32 s52, v254, 0
	v_readlane_b32 s53, v254, 1
	v_readlane_b32 s54, v254, 2
	v_readlane_b32 s55, v254, 3
	s_cbranch_execz .LBB0_1685
	v_ashrrev_i32_e32 v3, 31, v2
	v_lshl_add_u32 v6, v2, 2, 0
	v_lshl_add_u64 v[4:5], v[2:3], 2, s[42:43]
	s_mov_b64 s[6:7], 0
	v_mov_b32_e32 v3, v2
